# P6 epilogue: residual-x loads of row groups 1-3 issued one group ahead into free VGPRs (flat->global, counted vmcnt), on top of v21
# baseline (speedup 1.0000x reference)
.LBB0_820:
	ds_read_b128 v[130:133], v159
	ds_read_b128 v[134:137], v159 offset:1024
	ds_read_b128 v[138:141], v159 offset:2048
	ds_read_b128 v[142:145], v159 offset:3072
	s_add_i32 s14, s20, 0xfffb0080
	s_cmp_eq_u32 s49, 16
	s_cselect_b32 s52, s1, s14
	s_cselect_b32 s50, s0, s21
	s_or_b32 s51, s52, 0x80
	s_mov_b32 m0, s38
	ds_read_b128 v[146:149], v160
	ds_read_b128 v[150:153], v160 offset:1024
	ds_read_b128 v[166:169], v160 offset:2048
	ds_read_b128 v[170:173], v160 offset:3072
	ds_read_b128 v[174:177], v160 offset:4096
	ds_read_b128 v[178:181], v160 offset:5120
	ds_read_b128 v[182:185], v160 offset:6144
	ds_read_b128 v[186:189], v160 offset:7168
	buffer_load_dwordx4 v155, s[8:11], s20 offen lds
	s_mov_b32 m0, s39
	s_nop 0
	buffer_load_dwordx4 v156, s[8:11], s20 offen lds
	s_waitcnt lgkmcnt(8)
	s_barrier
	s_waitcnt lgkmcnt(0)
	s_setprio 1
	s_waitcnt lgkmcnt(6)
	v_mfma_f32_16x16x128_f8f6f4 v[126:129], v[130:137], v[146:153], v[126:129]
	v_mfma_f32_16x16x128_f8f6f4 v[122:125], v[138:145], v[146:153], v[122:125]
	s_waitcnt lgkmcnt(4)
	v_mfma_f32_16x16x128_f8f6f4 v[190:193], v[130:137], v[166:173], v[110:113]
	v_mfma_f32_16x16x128_f8f6f4 v[194:197], v[138:145], v[166:173], v[106:109]
	s_waitcnt lgkmcnt(2)
	v_mfma_f32_16x16x128_f8f6f4 v[198:201], v[130:137], v[174:181], v[94:97]
	v_mfma_f32_16x16x128_f8f6f4 v[202:205], v[138:145], v[174:181], v[90:93]
	s_waitcnt lgkmcnt(0)
	v_mfma_f32_16x16x128_f8f6f4 v[206:209], v[130:137], v[182:189], v[78:81]
	v_mfma_f32_16x16x128_f8f6f4 v[210:213], v[138:145], v[182:189], v[74:77]
	s_setprio 0
	s_barrier
	s_mov_b32 s14, s10
	s_mov_b32 s15, s11
	s_mov_b32 m0, s23
	s_nop 1
	ds_read_b128 v[74:77], v161
	ds_read_b128 v[78:81], v161 offset:1024
	ds_read_b128 v[90:93], v161 offset:2048
	ds_read_b128 v[94:97], v161 offset:3072
	buffer_load_dwordx4 v1, s[12:15], s50 offen lds
	s_mov_b32 m0, s24
	s_nop 0
	buffer_load_dwordx4 v154, s[12:15], s50 offen lds
	s_barrier
	s_waitcnt lgkmcnt(0)
	s_setprio 1
	s_waitcnt lgkmcnt(2)
	v_mfma_f32_16x16x128_f8f6f4 v[118:121], v[74:81], v[146:153], v[118:121]
	s_waitcnt lgkmcnt(0)
	v_mfma_f32_16x16x128_f8f6f4 v[114:117], v[90:97], v[146:153], v[114:117]
	v_mfma_f32_16x16x128_f8f6f4 v[146:149], v[74:81], v[166:173], v[102:105]
	v_mfma_f32_16x16x128_f8f6f4 v[150:153], v[90:97], v[166:173], v[98:101]
	v_mfma_f32_16x16x128_f8f6f4 v[166:169], v[74:81], v[174:181], v[86:89]
	v_mfma_f32_16x16x128_f8f6f4 v[170:173], v[90:97], v[174:181], v[82:85]
	v_mfma_f32_16x16x128_f8f6f4 v[174:177], v[74:81], v[182:189], v[70:73]
	v_mfma_f32_16x16x128_f8f6f4 v[178:181], v[90:97], v[182:189], v[66:69]
	s_setprio 0
	s_mov_b32 m0, s22
	s_barrier
	s_nop 3
	ds_read_b128 v[66:69], v160 offset:16384
	ds_read_b128 v[70:73], v160 offset:17408
	ds_read_b128 v[82:85], v160 offset:18432
	ds_read_b128 v[86:89], v160 offset:19456
	ds_read_b128 v[98:101], v160 offset:20480
	ds_read_b128 v[102:105], v160 offset:21504
	ds_read_b128 v[106:109], v160 offset:22528
	ds_read_b128 v[110:113], v160 offset:23552
	buffer_load_dwordx4 v155, s[8:11], s52 offen lds
	s_mov_b32 m0, s25
	s_nop 0
	buffer_load_dwordx4 v156, s[8:11], s52 offen lds
	s_barrier
	s_waitcnt lgkmcnt(0)
	s_setprio 1
	s_waitcnt lgkmcnt(6)
	v_mfma_f32_16x16x128_f8f6f4 v[62:65], v[130:137], v[66:73], v[62:65]
	v_mfma_f32_16x16x128_f8f6f4 v[58:61], v[138:145], v[66:73], v[58:61]
	s_waitcnt lgkmcnt(4)
	v_mfma_f32_16x16x128_f8f6f4 v[182:185], v[130:137], v[82:89], v[46:49]
	v_mfma_f32_16x16x128_f8f6f4 v[186:189], v[138:145], v[82:89], v[42:45]
	s_waitcnt lgkmcnt(2)
	v_mfma_f32_16x16x128_f8f6f4 v[214:217], v[130:137], v[98:105], v[22:25]
	v_mfma_f32_16x16x128_f8f6f4 v[218:221], v[138:145], v[98:105], v[18:21]
	s_waitcnt lgkmcnt(0)
	v_mfma_f32_16x16x128_f8f6f4 v[222:225], v[130:137], v[106:113], v[6:9]
	v_mfma_f32_16x16x128_f8f6f4 v[226:229], v[138:145], v[106:113], v[2:5]
	s_setprio 0
	s_barrier
	s_add_i32 s53, s50, 0x50000
	s_mov_b32 m0, s26
	s_nop 0
	buffer_load_dwordx4 v1, s[12:15], s53 offen lds
	s_mov_b32 m0, s27
	s_nop 0
	buffer_load_dwordx4 v154, s[12:15], s53 offen lds
	s_waitcnt vmcnt(6)
	s_barrier
	s_setprio 1
	v_mfma_f32_16x16x128_f8f6f4 v[54:57], v[74:81], v[66:73], v[54:57]
	v_mfma_f32_16x16x128_f8f6f4 v[50:53], v[90:97], v[66:73], v[50:53]
	v_mfma_f32_16x16x128_f8f6f4 v[230:233], v[74:81], v[82:89], v[38:41]
	v_mfma_f32_16x16x128_f8f6f4 v[234:237], v[90:97], v[82:89], v[34:37]
	v_mfma_f32_16x16x128_f8f6f4 v[238:241], v[74:81], v[98:105], v[30:33]
	v_mfma_f32_16x16x128_f8f6f4 v[242:245], v[90:97], v[98:105], v[26:29]
	v_mfma_f32_16x16x128_f8f6f4 v[246:249], v[74:81], v[106:113], v[14:17]
	v_mfma_f32_16x16x128_f8f6f4 v[250:253], v[90:97], v[106:113], v[10:13]
	s_setprio 0
	s_barrier
	ds_read_b128 v[2:5], v162
	ds_read_b128 v[6:9], v162 offset:1024
	s_nop 2
	ds_read_b128 v[10:13], v162 offset:2048
	ds_read_b128 v[14:17], v162 offset:3072
	s_add_i32 s52, s52, 0x50000
	s_mov_b32 m0, s28
	ds_read_b128 v[18:21], v160 offset:32768
	ds_read_b128 v[22:25], v160 offset:33792
	ds_read_b128 v[26:29], v160 offset:34816
	ds_read_b128 v[30:33], v160 offset:35840
	ds_read_b128 v[34:37], v160 offset:36864
	ds_read_b128 v[38:41], v160 offset:37888
	ds_read_b128 v[42:45], v160 offset:38912
	ds_read_b128 v[46:49], v160 offset:39936
	buffer_load_dwordx4 v155, s[8:11], s52 offen lds
	s_mov_b32 m0, s29
	s_nop 0
	buffer_load_dwordx4 v156, s[8:11], s52 offen lds
	s_waitcnt lgkmcnt(8)
	s_barrier
;     ...
;         if (FP8 == 2) { for (int t = 0; t < 8; t += 2) PG8_ITER(false); for (int t = 8; t < nt; t += 2) PG8_ITER(true); }
;         else { for (int t = 0; t < nt; t += 2) PG8_ITER(FP8 == 1); }
	s_waitcnt lgkmcnt(0)
	s_setprio 1
	s_waitcnt lgkmcnt(6)
	v_mfma_f32_16x16x128_f8f6f4 v[126:129], v[2:9], v[18:25], v[126:129]
	v_mfma_f32_16x16x128_f8f6f4 v[122:125], v[10:17], v[18:25], v[122:125]
	s_waitcnt lgkmcnt(4)
	v_mfma_f32_16x16x128_f8f6f4 v[110:113], v[2:9], v[26:33], v[190:193]
	v_mfma_f32_16x16x128_f8f6f4 v[106:109], v[10:17], v[26:33], v[194:197]
	s_waitcnt lgkmcnt(2)
	v_mfma_f32_16x16x128_f8f6f4 v[94:97], v[2:9], v[34:41], v[198:201]
	v_mfma_f32_16x16x128_f8f6f4 v[90:93], v[10:17], v[34:41], v[202:205]
	s_waitcnt lgkmcnt(0)
	v_mfma_f32_16x16x128_f8f6f4 v[78:81], v[2:9], v[42:49], v[206:209]
	v_mfma_f32_16x16x128_f8f6f4 v[74:77], v[10:17], v[42:49], v[210:213]
	s_setprio 0
	s_barrier
	s_or_b32 s52, s50, 0x80
	s_mov_b32 m0, s31
	ds_read_b128 v[130:133], v163
	ds_read_b128 v[134:137], v163 offset:1024
	ds_read_b128 v[138:141], v163 offset:2048
	ds_read_b128 v[142:145], v163 offset:3072
	buffer_load_dwordx4 v1, s[12:15], s52 offen lds
	s_mov_b32 m0, s33
	s_nop 0
	buffer_load_dwordx4 v154, s[12:15], s52 offen lds
	s_barrier
	s_waitcnt lgkmcnt(0)
	s_setprio 1
	s_waitcnt lgkmcnt(2)
	v_mfma_f32_16x16x128_f8f6f4 v[118:121], v[130:137], v[18:25], v[118:121]
	s_waitcnt lgkmcnt(0)
	v_mfma_f32_16x16x128_f8f6f4 v[114:117], v[138:145], v[18:25], v[114:117]
	v_mfma_f32_16x16x128_f8f6f4 v[102:105], v[130:137], v[26:33], v[146:149]
	v_mfma_f32_16x16x128_f8f6f4 v[98:101], v[138:145], v[26:33], v[150:153]
	v_mfma_f32_16x16x128_f8f6f4 v[86:89], v[130:137], v[34:41], v[166:169]
	v_mfma_f32_16x16x128_f8f6f4 v[82:85], v[138:145], v[34:41], v[170:173]
	v_mfma_f32_16x16x128_f8f6f4 v[70:73], v[130:137], v[42:49], v[174:177]
	v_mfma_f32_16x16x128_f8f6f4 v[66:69], v[138:145], v[42:49], v[178:181]
	s_setprio 0
	s_mov_b32 m0, s34
	s_barrier
	ds_read_b128 v[26:29], v160 offset:49152
	ds_read_b128 v[30:33], v160 offset:50176
	ds_read_b128 v[146:149], v160 offset:51200
	ds_read_b128 v[150:153], v160 offset:52224
	ds_read_b128 v[166:169], v160 offset:53248
	ds_read_b128 v[170:173], v160 offset:54272
	ds_read_b128 v[174:177], v160 offset:55296
	ds_read_b128 v[178:181], v160 offset:56320
	buffer_load_dwordx4 v155, s[8:11], s51 offen lds
	s_mov_b32 m0, s35
	s_nop 0
	buffer_load_dwordx4 v156, s[8:11], s51 offen lds
	s_barrier
	s_waitcnt lgkmcnt(0)
	s_setprio 1
	s_waitcnt lgkmcnt(6)
	v_mfma_f32_16x16x128_f8f6f4 v[62:65], v[2:9], v[26:33], v[62:65]
	v_mfma_f32_16x16x128_f8f6f4 v[58:61], v[10:17], v[26:33], v[58:61]
	s_waitcnt lgkmcnt(4)
	v_mfma_f32_16x16x128_f8f6f4 v[46:49], v[2:9], v[146:153], v[182:185]
	v_mfma_f32_16x16x128_f8f6f4 v[42:45], v[10:17], v[146:153], v[186:189]
	s_waitcnt lgkmcnt(2)
	v_mfma_f32_16x16x128_f8f6f4 v[22:25], v[2:9], v[166:173], v[214:217]
	v_mfma_f32_16x16x128_f8f6f4 v[18:21], v[10:17], v[166:173], v[218:221]
	s_waitcnt lgkmcnt(0)
	v_mfma_f32_16x16x128_f8f6f4 v[6:9], v[2:9], v[174:181], v[222:225]
	v_mfma_f32_16x16x128_f8f6f4 v[2:5], v[10:17], v[174:181], v[226:229]
	s_setprio 0
	s_barrier
	s_add_i32 s50, s50, 0x50080
	s_mov_b32 m0, s36
	s_nop 0
	buffer_load_dwordx4 v1, s[12:15], s50 offen lds
	s_mov_b32 m0, s37
	s_nop 0
	buffer_load_dwordx4 v154, s[12:15], s50 offen lds
	s_waitcnt vmcnt(6)
	s_barrier
	s_setprio 1
	v_mfma_f32_16x16x128_f8f6f4 v[54:57], v[130:137], v[26:33], v[54:57]
	v_mfma_f32_16x16x128_f8f6f4 v[50:53], v[138:145], v[26:33], v[50:53]
	v_mfma_f32_16x16x128_f8f6f4 v[38:41], v[130:137], v[146:153], v[230:233]
	v_mfma_f32_16x16x128_f8f6f4 v[34:37], v[138:145], v[146:153], v[234:237]
	v_mfma_f32_16x16x128_f8f6f4 v[30:33], v[130:137], v[166:173], v[238:241]
	v_mfma_f32_16x16x128_f8f6f4 v[26:29], v[138:145], v[166:173], v[242:245]
	v_mfma_f32_16x16x128_f8f6f4 v[14:17], v[130:137], v[174:181], v[246:249]
	v_mfma_f32_16x16x128_f8f6f4 v[10:13], v[138:145], v[174:181], v[250:253]
	s_setprio 0
	s_add_i32 s49, s49, 2
	s_addk_i32 s20, 0x100
	s_addk_i32 s21, 0x100
	s_cmp_gt_u32 s49, 17
	s_barrier
	s_cbranch_scc0 .LBB0_820
; #define LAS __attribute__((address_space(3)))
;     __device__ __forceinline__ void operator()(const f32x4 (&acc)[2][2][4][2], const Unit& u, int wr, int wc, int fr, int fq, LAS const unsigned char* tbl, LAS const unsigned char* b2l) const {
;         const int row0 = u.pm * BM + wr * 64 + fr, col0 = u.pn * BM + wc * 32 + 8 * fq;
;         const float* __restrict__ rp = args_in(ka, 0); _Float16* __restrict__ cp = (_Float16*)(ws + WS_X1H); float* rowss = (float*)(ws + rowss_off);
; #pragma unroll
;         for (int ai = 0; ai < 2; ++ai)
; #pragma unroll
;             for (int mp = 0; mp < 2; ++mp) { f32x4 r[2][2][2];
; #pragma unroll
;                 for (int mm = 0; mm < 2; ++mm) { const size_t off = (size_t)(row0 + ai * HALF + (2 * mp + mm) * 16) * ldc + col0;
; #pragma unroll
;                     for (int bj = 0; bj < 2; ++bj)
; #pragma unroll
;                         for (int n = 0; n < 2; ++n) r[mm][bj][n] = __builtin_nontemporal_load((const f32x4*)(rp + off + bj * HALF + n * 4)); }
; #pragma unroll
;                 for (int mm = 0; mm < 2; ++mm) { const int m = 2 * mp + mm; const int row = row0 + ai * HALF + m * 16; const size_t off = (size_t)row * ldc + col0; float ss = 0.f;
; #pragma unroll
;                     for (int bj = 0; bj < 2; ++bj) { const f32x4 o0 = r[mm][bj][0] + acc[ai][bj][m][0] * scale, o1 = r[mm][bj][1] + acc[ai][bj][m][1] * scale;
;                         ss += ((o0[0] * o0[0] + o0[1] * o0[1]) + (o0[2] * o0[2] + o0[3] * o0[3])) + ((o1[0] * o1[0] + o1[1] * o1[1]) + (o1[2] * o1[2] + o1[3] * o1[3]));
;                         f16x8 h;
; #pragma unroll
;                         for (int j = 0; j < 4; ++j) { h[j] = (_Float16)__builtin_amdgcn_fmed3f(o0[j], -65504.0f, 65504.0f); h[4 + j] = (_Float16)__builtin_amdgcn_fmed3f(o1[j], -65504.0f, 65504.0f); }
;                         *(f16x8*)(cp + off + bj * HALF) = h; }
;                     ss += __shfl_xor(ss, 16); ss += __shfl_xor(ss, 32);
;                     if (fq == 0) rowss[(size_t)row * 32 + u.pn * 4 + wc] = ss; } }
	v_mov_b64_e32 v[130:131], s[54:55]
	flat_load_dwordx2 v[130:131], v[130:131]
	v_lshl_add_u32 v148, s46, 8, v157
	v_lshl_or_b32 v146, s45, 8, v158
	v_ashrrev_i32_e32 v147, 31, v146
	v_ashrrev_i32_e32 v149, 31, v148
	v_lshlrev_b64 v[132:133], 13, v[148:149]
	v_or_b32_e32 v152, 16, v148
	v_ashrrev_i32_e32 v153, 31, v152
	v_and_b32_e32 v167, 64, v164
	v_xor_b32_e32 v166, 16, v164
	v_add_u32_e32 v167, 64, v167
	v_xor_b32_e32 v184, 32, v164
	v_cmp_lt_i32_e32 vcc, v166, v167
	s_lshl_b32 s0, s45, 2
	s_ashr_i32 s1, s0, 31
	v_cndmask_b32_e32 v166, v164, v166, vcc
	v_cmp_lt_i32_e32 vcc, v184, v167
	v_lshlrev_b32_e32 v167, 2, v166
	s_lshl_b64 s[0:1], s[0:1], 2
	v_cndmask_b32_e32 v186, v164, v184, vcc
	v_lshlrev_b64 v[184:185], 12, v[148:149]
	v_lshlrev_b32_e32 v166, 2, v186
	s_add_u32 s14, s40, s0
	s_addc_u32 s15, s41, s1
	s_waitcnt vmcnt(0) lgkmcnt(0)
	v_lshl_add_u64 v[150:151], v[146:147], 2, v[130:131]
	v_lshl_add_u64 v[130:131], v[150:151], 0, v[132:133]
	global_load_dwordx4 v[168:171], v[130:131], off nt
	global_load_dwordx4 v[172:175], v[130:131], off offset:16 nt
	global_load_dwordx4 v[176:179], v[130:131], off offset:512 nt
	global_load_dwordx4 v[180:183], v[130:131], off offset:528 nt
	v_lshlrev_b64 v[130:131], 13, v[152:153]
	v_lshl_add_u64 v[130:131], v[150:151], 0, v[130:131]
	global_load_dwordx4 v[142:145], v[130:131], off nt
	global_load_dwordx4 v[138:141], v[130:131], off offset:16 nt
	global_load_dwordx4 v[134:137], v[130:131], off offset:512 nt
	s_nop 0
	global_load_dwordx4 v[130:133], v[130:131], off offset:528 nt
	v_lshl_add_u64 v[146:147], v[146:147], 1, s[2:3]
	v_lshl_add_u64 v[184:185], v[146:147], 0, v[184:185]
	s_waitcnt vmcnt(0) lgkmcnt(0)
	v_add_u32_e32 v188, 0x20, v148
	v_ashrrev_i32_e32 v189, 31, v188
	v_lshlrev_b64 v[188:189], 13, v[188:189]
	v_lshl_add_u64 v[188:189], v[150:151], 0, v[188:189]
	global_load_dwordx4 v[190:193], v[188:189], off nt
	global_load_dwordx4 v[194:197], v[188:189], off offset:16 nt
	global_load_dwordx4 v[198:201], v[188:189], off offset:512 nt
	global_load_dwordx4 v[202:205], v[188:189], off offset:528 nt
	v_add_u32_e32 v188, 0x30, v148
	v_ashrrev_i32_e32 v189, 31, v188
	v_lshlrev_b64 v[188:189], 13, v[188:189]
	v_lshl_add_u64 v[188:189], v[150:151], 0, v[188:189]
	global_load_dwordx4 v[206:209], v[188:189], off nt
	global_load_dwordx4 v[210:213], v[188:189], off offset:16 nt
	global_load_dwordx4 v[214:217], v[188:189], off offset:512 nt
	global_load_dwordx4 v[218:221], v[188:189], off offset:528 nt
	v_pk_fma_f32 v[128:129], v[128:129], s[16:17], v[170:171] op_sel_hi:[1,0,1]
	v_pk_fma_f32 v[126:127], v[126:127], s[16:17], v[168:169] op_sel_hi:[1,0,1]
	v_pk_fma_f32 v[124:125], v[124:125], s[16:17], v[174:175] op_sel_hi:[1,0,1]
	v_pk_fma_f32 v[122:123], v[122:123], s[16:17], v[172:173] op_sel_hi:[1,0,1]
	v_pk_fma_f32 v[120:121], v[120:121], s[16:17], v[178:179] op_sel_hi:[1,0,1]
	v_pk_fma_f32 v[118:119], v[118:119], s[16:17], v[176:177] op_sel_hi:[1,0,1]
	v_pk_fma_f32 v[168:169], v[116:117], s[16:17], v[182:183] op_sel_hi:[1,0,1]
	v_pk_fma_f32 v[170:171], v[114:115], s[16:17], v[180:181] op_sel_hi:[1,0,1]
	v_mul_f32_e32 v172, v127, v127
	v_mul_f32_e32 v173, v129, v129
	v_mul_f32_e32 v174, v123, v123
	v_mul_f32_e32 v175, v125, v125
	v_med3_f32 v114, v126, s42, v165
	v_med3_f32 v116, v122, s42, v165
	v_med3_f32 v127, v127, s42, v165
	v_med3_f32 v123, v123, s42, v165
	v_med3_f32 v115, v128, s42, v165
	v_med3_f32 v117, v124, s42, v165
	v_med3_f32 v129, v129, s42, v165
	v_med3_f32 v125, v125, s42, v165
	v_mul_f32_e32 v176, v119, v119
	v_mul_f32_e32 v177, v121, v121
	v_mul_f32_e32 v178, v171, v171
	v_mul_f32_e32 v179, v169, v169
	v_fmac_f32_e32 v172, v126, v126
	v_fmac_f32_e32 v173, v128, v128
	v_fmac_f32_e32 v174, v122, v122
	v_fmac_f32_e32 v175, v124, v124
	v_cvt_pk_f16_f32 v117, v117, v125
	v_cvt_pk_f16_f32 v115, v115, v129
	v_cvt_pk_f16_f32 v116, v116, v123
	v_cvt_pk_f16_f32 v114, v114, v127
	v_fmac_f32_e32 v176, v118, v118
	v_fmac_f32_e32 v177, v120, v120
	v_fmac_f32_e32 v178, v170, v170
	v_fmac_f32_e32 v179, v168, v168
	v_med3_f32 v180, v118, s42, v165
	v_med3_f32 v182, v119, s42, v165
	v_add_f32_e32 v118, v172, v173
	v_add_f32_e32 v119, v174, v175
	global_store_dwordx4 v[184:185], v[114:117], off
	v_med3_f32 v181, v170, s42, v165
	v_med3_f32 v171, v171, s42, v165
	v_add_f32_e32 v114, v176, v177
	v_add_f32_e32 v115, v178, v179
	v_add_f32_e32 v116, v118, v119
	v_add_f32_e32 v114, v114, v115
	v_add_f32_e32 v114, v116, v114
	ds_bpermute_b32 v115, v167, v114
	v_med3_f32 v117, v120, s42, v165
	v_med3_f32 v116, v168, s42, v165
	v_med3_f32 v118, v121, s42, v165
	v_med3_f32 v119, v169, s42, v165
	s_waitcnt lgkmcnt(0)
	v_add_f32_e32 v114, v114, v115
	ds_bpermute_b32 v115, v166, v114
	v_cvt_pk_f16_f32 v119, v116, v119
	v_cvt_pk_f16_f32 v117, v117, v118
	v_cvt_pk_f16_f32 v118, v181, v171
	v_cvt_pk_f16_f32 v116, v180, v182
	global_store_dwordx4 v[184:185], v[116:119], off offset:256
	s_and_saveexec_b64 s[0:1], s[6:7]
	s_cbranch_execz .LBB0_823
	v_lshlrev_b64 v[116:117], 7, v[148:149]
	v_lshl_add_u64 v[116:117], s[14:15], 0, v[116:117]
	s_waitcnt lgkmcnt(0)
	v_add_f32_e32 v114, v114, v115
	global_store_dword v[116:117], v114, off

;     __device__ __forceinline__ void operator()(const f32x4 (&acc)[2][2][4][2], const Unit& u, int wr, int wc, int fr, int fq, LAS const unsigned char* tbl, LAS const unsigned char* b2l) const {
;     ...
;             for (int mp = 0; mp < 2; ++mp) { f32x4 r[2][2][2];
; #pragma unroll
;                 for (int mm = 0; mm < 2; ++mm) { const size_t off = (size_t)(row0 + ai * HALF + (2 * mp + mm) * 16) * ldc + col0;
; #pragma unroll
;                     for (int bj = 0; bj < 2; ++bj)
; #pragma unroll
;                         for (int n = 0; n < 2; ++n) r[mm][bj][n] = __builtin_nontemporal_load((const f32x4*)(rp + off + bj * HALF + n * 4)); }
; #pragma unroll
;                 for (int mm = 0; mm < 2; ++mm) { const int m = 2 * mp + mm; const int row = row0 + ai * HALF + m * 16; const size_t off = (size_t)row * ldc + col0; float ss = 0.f;
; #pragma unroll
;                     for (int bj = 0; bj < 2; ++bj) { const f32x4 o0 = r[mm][bj][0] + acc[ai][bj][m][0] * scale, o1 = r[mm][bj][1] + acc[ai][bj][m][1] * scale;
;                         ss += ((o0[0] * o0[0] + o0[1] * o0[1]) + (o0[2] * o0[2] + o0[3] * o0[3])) + ((o1[0] * o1[0] + o1[1] * o1[1]) + (o1[2] * o1[2] + o1[3] * o1[3]));
;                         f16x8 h;
; #pragma unroll
;                         for (int j = 0; j < 4; ++j) { h[j] = (_Float16)__builtin_amdgcn_fmed3f(o0[j], -65504.0f, 65504.0f); h[4 + j] = (_Float16)__builtin_amdgcn_fmed3f(o1[j], -65504.0f, 65504.0f); }
;                         *(f16x8*)(cp + off + bj * HALF) = h; }
;                     ss += __shfl_xor(ss, 16); ss += __shfl_xor(ss, 32);
;                     if (fq == 0) rowss[(size_t)row * 32 + u.pn * 4 + wc] = ss; } }
.LBB0_825:
	s_or_b64 exec, exec, s[0:1]
	v_or_b32_e32 v116, 32, v148
	v_ashrrev_i32_e32 v117, 31, v116
	s_waitcnt lgkmcnt(0)
	v_lshlrev_b64 v[98:99], 13, v[116:117]
	v_lshl_add_u64 v[98:99], v[150:151], 0, v[98:99]
	v_or_b32_e32 v114, 48, v148
	v_ashrrev_i32_e32 v115, 31, v114
	v_lshlrev_b64 v[98:99], 13, v[114:115]
	v_lshl_add_u64 v[98:99], v[150:151], 0, v[98:99]
	v_lshlrev_b64 v[134:135], 12, v[116:117]
	v_lshl_add_u64 v[134:135], v[146:147], 0, v[134:135]
	s_waitcnt vmcnt(4) lgkmcnt(0)
	v_add_u32_e32 v188, 0x80, v148
	v_ashrrev_i32_e32 v189, 31, v188
	v_lshlrev_b64 v[188:189], 13, v[188:189]
	v_lshl_add_u64 v[188:189], v[150:151], 0, v[188:189]
	global_load_dwordx4 v[222:225], v[188:189], off nt
	global_load_dwordx4 v[226:229], v[188:189], off offset:16 nt
	global_load_dwordx4 v[230:233], v[188:189], off offset:512 nt
	global_load_dwordx4 v[234:237], v[188:189], off offset:528 nt
	v_add_u32_e32 v188, 0x90, v148
	v_ashrrev_i32_e32 v189, 31, v188
	v_lshlrev_b64 v[188:189], 13, v[188:189]
	v_lshl_add_u64 v[188:189], v[150:151], 0, v[188:189]
	global_load_dwordx4 v[238:241], v[188:189], off nt
	global_load_dwordx4 v[242:245], v[188:189], off offset:16 nt
	global_load_dwordx4 v[246:249], v[188:189], off offset:512 nt
	global_load_dwordx4 v[250:253], v[188:189], off offset:528 nt
	v_pk_fma_f32 v[96:97], v[96:97], s[16:17], v[192:193] op_sel_hi:[1,0,1]
	v_pk_fma_f32 v[94:95], v[94:95], s[16:17], v[190:191] op_sel_hi:[1,0,1]
	v_pk_fma_f32 v[92:93], v[92:93], s[16:17], v[196:197] op_sel_hi:[1,0,1]
	v_pk_fma_f32 v[90:91], v[90:91], s[16:17], v[194:195] op_sel_hi:[1,0,1]
	v_pk_fma_f32 v[88:89], v[88:89], s[16:17], v[200:201] op_sel_hi:[1,0,1]
	v_pk_fma_f32 v[86:87], v[86:87], s[16:17], v[198:199] op_sel_hi:[1,0,1]
	v_pk_fma_f32 v[118:119], v[84:85], s[16:17], v[204:205] op_sel_hi:[1,0,1]
	v_pk_fma_f32 v[120:121], v[82:83], s[16:17], v[202:203] op_sel_hi:[1,0,1]
	v_mul_f32_e32 v122, v95, v95
	v_mul_f32_e32 v123, v97, v97
	v_mul_f32_e32 v124, v91, v91
	v_mul_f32_e32 v125, v93, v93
	v_med3_f32 v82, v94, s42, v165
	v_med3_f32 v84, v90, s42, v165
	v_med3_f32 v95, v95, s42, v165
	v_med3_f32 v91, v91, s42, v165
	v_med3_f32 v83, v96, s42, v165
	v_med3_f32 v85, v92, s42, v165
	v_med3_f32 v97, v97, s42, v165
	v_med3_f32 v93, v93, s42, v165
	v_mul_f32_e32 v126, v87, v87
	v_mul_f32_e32 v127, v89, v89
	v_mul_f32_e32 v128, v121, v121
	v_mul_f32_e32 v129, v119, v119
	v_fmac_f32_e32 v122, v94, v94
	v_fmac_f32_e32 v123, v96, v96
	v_fmac_f32_e32 v124, v90, v90
	v_fmac_f32_e32 v125, v92, v92
	v_cvt_pk_f16_f32 v85, v85, v93
	v_cvt_pk_f16_f32 v83, v83, v97
	v_cvt_pk_f16_f32 v84, v84, v91
	v_cvt_pk_f16_f32 v82, v82, v95
	v_fmac_f32_e32 v126, v86, v86
	v_fmac_f32_e32 v127, v88, v88
	v_fmac_f32_e32 v128, v120, v120
	v_fmac_f32_e32 v129, v118, v118
	v_med3_f32 v130, v86, s42, v165
	v_med3_f32 v132, v87, s42, v165
	v_add_f32_e32 v86, v122, v123
	v_add_f32_e32 v87, v124, v125
	global_store_dwordx4 v[134:135], v[82:85], off
	v_med3_f32 v131, v120, s42, v165
	v_med3_f32 v121, v121, s42, v165
	v_add_f32_e32 v82, v126, v127
	v_add_f32_e32 v83, v128, v129
	v_add_f32_e32 v84, v86, v87
	v_add_f32_e32 v82, v82, v83
	v_add_f32_e32 v82, v84, v82
	ds_bpermute_b32 v83, v167, v82
	v_med3_f32 v85, v88, s42, v165
	v_med3_f32 v84, v118, s42, v165
	v_med3_f32 v86, v89, s42, v165
	v_med3_f32 v87, v119, s42, v165
	s_waitcnt lgkmcnt(0)
	v_add_f32_e32 v82, v82, v83
	ds_bpermute_b32 v83, v166, v82
	v_cvt_pk_f16_f32 v87, v84, v87
	v_cvt_pk_f16_f32 v85, v85, v86
	v_cvt_pk_f16_f32 v86, v131, v121
	v_cvt_pk_f16_f32 v84, v130, v132
	global_store_dwordx4 v[134:135], v[84:87], off offset:256
	s_and_saveexec_b64 s[0:1], s[6:7]
	s_cbranch_execz .LBB0_827
	v_lshlrev_b64 v[84:85], 7, v[116:117]
	v_lshl_add_u64 v[84:85], s[14:15], 0, v[84:85]
	s_waitcnt lgkmcnt(0)
	v_add_f32_e32 v82, v82, v83
	global_store_dword v[84:85], v82, off
.LBB0_827:
	s_or_b64 exec, exec, s[0:1]
	v_pk_fma_f32 v[80:81], v[80:81], s[16:17], v[208:209] op_sel_hi:[1,0,1]
	v_pk_fma_f32 v[78:79], v[78:79], s[16:17], v[206:207] op_sel_hi:[1,0,1]
	v_mul_f32_e32 v85, v81, v81
	v_mul_f32_e32 v84, v79, v79
	v_pk_fma_f32 v[76:77], v[76:77], s[16:17], v[212:213] op_sel_hi:[1,0,1]
	v_pk_fma_f32 v[74:75], v[74:75], s[16:17], v[210:211] op_sel_hi:[1,0,1]
	v_fmac_f32_e32 v84, v78, v78
	v_fmac_f32_e32 v85, v80, v80
	v_add_f32_e32 v84, v84, v85
	v_mul_f32_e32 v85, v75, v75
	v_mul_f32_e32 v86, v77, v77
	v_fmac_f32_e32 v85, v74, v74
	v_fmac_f32_e32 v86, v76, v76
	v_add_f32_e32 v85, v85, v86
	s_waitcnt lgkmcnt(0)
	v_lshlrev_b64 v[82:83], 11, v[114:115]
	v_add_f32_e32 v84, v84, v85
	v_med3_f32 v78, v78, s42, v165
	v_med3_f32 v74, v74, s42, v165
	v_med3_f32 v79, v79, s42, v165
	v_med3_f32 v85, v75, s42, v165
	v_med3_f32 v75, v80, s42, v165
	v_med3_f32 v76, v76, s42, v165
	v_med3_f32 v80, v81, s42, v165
	v_med3_f32 v77, v77, s42, v165
	v_lshl_add_u64 v[82:83], v[82:83], 1, v[146:147]
	v_cvt_pk_f16_f32 v77, v76, v77
	v_cvt_pk_f16_f32 v75, v75, v80
	v_cvt_pk_f16_f32 v76, v74, v85
	v_cvt_pk_f16_f32 v74, v78, v79
	v_pk_fma_f32 v[72:73], v[72:73], s[16:17], v[216:217] op_sel_hi:[1,0,1]
	v_pk_fma_f32 v[70:71], v[70:71], s[16:17], v[214:215] op_sel_hi:[1,0,1]
	global_store_dwordx4 v[82:83], v[74:77], off
	v_pk_fma_f32 v[68:69], v[68:69], s[16:17], v[220:221] op_sel_hi:[1,0,1]
	v_pk_fma_f32 v[66:67], v[66:67], s[16:17], v[218:219] op_sel_hi:[1,0,1]
	v_mul_f32_e32 v74, v71, v71
	v_mul_f32_e32 v75, v73, v73
	v_fmac_f32_e32 v74, v70, v70
	v_fmac_f32_e32 v75, v72, v72
	v_add_f32_e32 v74, v74, v75
	v_mul_f32_e32 v75, v67, v67
	v_mul_f32_e32 v76, v69, v69
	v_fmac_f32_e32 v75, v66, v66
	v_fmac_f32_e32 v76, v68, v68
	v_add_f32_e32 v75, v75, v76
	v_add_f32_e32 v74, v74, v75
	v_med3_f32 v75, v70, s42, v165
	v_med3_f32 v70, v66, s42, v165
	v_add_f32_e32 v66, v84, v74
	v_med3_f32 v77, v67, s42, v165
	ds_bpermute_b32 v67, v167, v66
	v_med3_f32 v76, v71, s42, v165
	v_med3_f32 v72, v72, s42, v165
	v_med3_f32 v68, v68, s42, v165
	v_med3_f32 v73, v73, s42, v165
	s_waitcnt lgkmcnt(0)
	v_add_f32_e32 v66, v66, v67
	ds_bpermute_b32 v67, v166, v66
	v_med3_f32 v69, v69, s42, v165
	v_cvt_pk_f16_f32 v71, v68, v69
	v_cvt_pk_f16_f32 v69, v72, v73
	v_cvt_pk_f16_f32 v70, v70, v77
	v_cvt_pk_f16_f32 v68, v75, v76
	global_store_dwordx4 v[82:83], v[68:71], off offset:256
	s_and_saveexec_b64 s[0:1], s[6:7]
	s_cbranch_execz .LBB0_829
	v_lshlrev_b64 v[68:69], 7, v[114:115]
	v_lshl_add_u64 v[68:69], s[14:15], 0, v[68:69]
	s_waitcnt lgkmcnt(0)
	v_add_f32_e32 v66, v66, v67
	global_store_dword v[68:69], v66, off
;     __device__ __forceinline__ void operator()(const f32x4 (&acc)[2][2][4][2], const Unit& u, int wr, int wc, int fr, int fq, LAS const unsigned char* tbl, LAS const unsigned char* b2l) const {
;     ...
;             for (int mp = 0; mp < 2; ++mp) { f32x4 r[2][2][2];
; #pragma unroll
;                 for (int mm = 0; mm < 2; ++mm) { const size_t off = (size_t)(row0 + ai * HALF + (2 * mp + mm) * 16) * ldc + col0;
; #pragma unroll
;                     for (int bj = 0; bj < 2; ++bj)
; #pragma unroll
;                         for (int n = 0; n < 2; ++n) r[mm][bj][n] = __builtin_nontemporal_load((const f32x4*)(rp + off + bj * HALF + n * 4)); }
; #pragma unroll
;                 for (int mm = 0; mm < 2; ++mm) { const int m = 2 * mp + mm; const int row = row0 + ai * HALF + m * 16; const size_t off = (size_t)row * ldc + col0; float ss = 0.f;
; #pragma unroll
;                     for (int bj = 0; bj < 2; ++bj) { const f32x4 o0 = r[mm][bj][0] + acc[ai][bj][m][0] * scale, o1 = r[mm][bj][1] + acc[ai][bj][m][1] * scale;
;                         ss += ((o0[0] * o0[0] + o0[1] * o0[1]) + (o0[2] * o0[2] + o0[3] * o0[3])) + ((o1[0] * o1[0] + o1[1] * o1[1]) + (o1[2] * o1[2] + o1[3] * o1[3]));
;                         f16x8 h;
; #pragma unroll
;                         for (int j = 0; j < 4; ++j) { h[j] = (_Float16)__builtin_amdgcn_fmed3f(o0[j], -65504.0f, 65504.0f); h[4 + j] = (_Float16)__builtin_amdgcn_fmed3f(o1[j], -65504.0f, 65504.0f); }
;                         *(f16x8*)(cp + off + bj * HALF) = h; }
;                     ss += __shfl_xor(ss, 16); ss += __shfl_xor(ss, 32);
;                     if (fq == 0) rowss[(size_t)row * 32 + u.pn * 4 + wc] = ss; } }
.LBB0_829:
	s_or_b64 exec, exec, s[0:1]
	v_add_u32_e32 v84, 0x80, v148
	v_ashrrev_i32_e32 v85, 31, v84
	s_waitcnt lgkmcnt(0)
	v_lshlrev_b64 v[66:67], 13, v[84:85]
	v_lshl_add_u64 v[66:67], v[150:151], 0, v[66:67]
	v_add_u32_e32 v82, 0x90, v148
	v_ashrrev_i32_e32 v83, 31, v82
	v_lshlrev_b64 v[66:67], 13, v[82:83]
	v_lshl_add_u64 v[66:67], v[150:151], 0, v[66:67]
	v_lshlrev_b64 v[102:103], 12, v[84:85]
	v_lshl_add_u64 v[102:103], v[146:147], 0, v[102:103]
	s_waitcnt vmcnt(4) lgkmcnt(0)
	v_add_u32_e32 v188, 0xa0, v148
	v_ashrrev_i32_e32 v189, 31, v188
	v_lshlrev_b64 v[188:189], 13, v[188:189]
	v_lshl_add_u64 v[188:189], v[150:151], 0, v[188:189]
	global_load_dwordx4 v[190:193], v[188:189], off nt
	global_load_dwordx4 v[194:197], v[188:189], off offset:16 nt
	global_load_dwordx4 v[198:201], v[188:189], off offset:512 nt
	global_load_dwordx4 v[202:205], v[188:189], off offset:528 nt
	v_add_u32_e32 v188, 0xb0, v148
	v_ashrrev_i32_e32 v189, 31, v188
	v_lshlrev_b64 v[188:189], 13, v[188:189]
	v_lshl_add_u64 v[188:189], v[150:151], 0, v[188:189]
	global_load_dwordx4 v[206:209], v[188:189], off nt
	global_load_dwordx4 v[210:213], v[188:189], off offset:16 nt
	global_load_dwordx4 v[214:217], v[188:189], off offset:512 nt
	global_load_dwordx4 v[218:221], v[188:189], off offset:528 nt
	v_pk_fma_f32 v[64:65], v[64:65], s[16:17], v[224:225] op_sel_hi:[1,0,1]
	v_pk_fma_f32 v[62:63], v[62:63], s[16:17], v[222:223] op_sel_hi:[1,0,1]
	v_pk_fma_f32 v[60:61], v[60:61], s[16:17], v[228:229] op_sel_hi:[1,0,1]
	v_pk_fma_f32 v[58:59], v[58:59], s[16:17], v[226:227] op_sel_hi:[1,0,1]
	v_pk_fma_f32 v[56:57], v[56:57], s[16:17], v[232:233] op_sel_hi:[1,0,1]
	v_pk_fma_f32 v[54:55], v[54:55], s[16:17], v[230:231] op_sel_hi:[1,0,1]
	v_pk_fma_f32 v[86:87], v[52:53], s[16:17], v[236:237] op_sel_hi:[1,0,1]
	v_pk_fma_f32 v[88:89], v[50:51], s[16:17], v[234:235] op_sel_hi:[1,0,1]
	v_mul_f32_e32 v90, v63, v63
	v_mul_f32_e32 v91, v65, v65
	v_mul_f32_e32 v92, v59, v59
	v_mul_f32_e32 v93, v61, v61
	v_med3_f32 v50, v62, s42, v165
	v_med3_f32 v52, v58, s42, v165
	v_med3_f32 v63, v63, s42, v165
	v_med3_f32 v59, v59, s42, v165
	v_med3_f32 v51, v64, s42, v165
	v_med3_f32 v53, v60, s42, v165
	v_med3_f32 v65, v65, s42, v165
	v_med3_f32 v61, v61, s42, v165
	v_mul_f32_e32 v94, v55, v55
	v_mul_f32_e32 v95, v57, v57
	v_mul_f32_e32 v96, v89, v89
	v_mul_f32_e32 v97, v87, v87
	v_fmac_f32_e32 v90, v62, v62
	v_fmac_f32_e32 v91, v64, v64
	v_fmac_f32_e32 v92, v58, v58
	v_fmac_f32_e32 v93, v60, v60
	v_cvt_pk_f16_f32 v53, v53, v61
	v_cvt_pk_f16_f32 v51, v51, v65
	v_cvt_pk_f16_f32 v52, v52, v59
	v_cvt_pk_f16_f32 v50, v50, v63
	v_fmac_f32_e32 v94, v54, v54
	v_fmac_f32_e32 v95, v56, v56
	v_fmac_f32_e32 v96, v88, v88
	v_fmac_f32_e32 v97, v86, v86
	v_med3_f32 v98, v54, s42, v165
	v_med3_f32 v100, v55, s42, v165
	v_add_f32_e32 v54, v90, v91
	v_add_f32_e32 v55, v92, v93
	global_store_dwordx4 v[102:103], v[50:53], off
	v_med3_f32 v99, v88, s42, v165
	v_med3_f32 v89, v89, s42, v165
	v_add_f32_e32 v50, v94, v95
	v_add_f32_e32 v51, v96, v97
	v_add_f32_e32 v52, v54, v55
	v_add_f32_e32 v50, v50, v51
	v_add_f32_e32 v50, v52, v50
	ds_bpermute_b32 v51, v167, v50
	v_med3_f32 v53, v56, s42, v165
	v_med3_f32 v52, v86, s42, v165
	v_med3_f32 v54, v57, s42, v165
	v_med3_f32 v55, v87, s42, v165
	s_waitcnt lgkmcnt(0)
	v_add_f32_e32 v50, v50, v51
	ds_bpermute_b32 v51, v166, v50
	v_cvt_pk_f16_f32 v55, v52, v55
	v_cvt_pk_f16_f32 v53, v53, v54
	v_cvt_pk_f16_f32 v54, v99, v89
	v_cvt_pk_f16_f32 v52, v98, v100
	global_store_dwordx4 v[102:103], v[52:55], off offset:256
	s_and_saveexec_b64 s[0:1], s[6:7]
	s_cbranch_execz .LBB0_831
	v_lshlrev_b64 v[52:53], 7, v[84:85]
	v_lshl_add_u64 v[52:53], s[14:15], 0, v[52:53]
	s_waitcnt lgkmcnt(0)
	v_add_f32_e32 v50, v50, v51
	global_store_dword v[52:53], v50, off
.LBB0_831:
	s_or_b64 exec, exec, s[0:1]
	v_pk_fma_f32 v[48:49], v[48:49], s[16:17], v[240:241] op_sel_hi:[1,0,1]
	v_pk_fma_f32 v[46:47], v[46:47], s[16:17], v[238:239] op_sel_hi:[1,0,1]
	v_mul_f32_e32 v53, v49, v49
	v_mul_f32_e32 v52, v47, v47
	v_pk_fma_f32 v[44:45], v[44:45], s[16:17], v[244:245] op_sel_hi:[1,0,1]
	v_pk_fma_f32 v[42:43], v[42:43], s[16:17], v[242:243] op_sel_hi:[1,0,1]
	v_fmac_f32_e32 v52, v46, v46
	v_fmac_f32_e32 v53, v48, v48
	v_add_f32_e32 v52, v52, v53
	v_mul_f32_e32 v53, v43, v43
	v_mul_f32_e32 v54, v45, v45
	v_fmac_f32_e32 v53, v42, v42
	v_fmac_f32_e32 v54, v44, v44
	v_add_f32_e32 v53, v53, v54
	s_waitcnt lgkmcnt(0)
	v_lshlrev_b64 v[50:51], 11, v[82:83]
	v_add_f32_e32 v52, v52, v53
	v_med3_f32 v46, v46, s42, v165
	v_med3_f32 v42, v42, s42, v165
	v_med3_f32 v47, v47, s42, v165
	v_med3_f32 v53, v43, s42, v165
	v_med3_f32 v43, v48, s42, v165
	v_med3_f32 v44, v44, s42, v165
	v_med3_f32 v48, v49, s42, v165
	v_med3_f32 v45, v45, s42, v165
	v_lshl_add_u64 v[50:51], v[50:51], 1, v[146:147]
	v_cvt_pk_f16_f32 v45, v44, v45
	v_cvt_pk_f16_f32 v43, v43, v48
	v_cvt_pk_f16_f32 v44, v42, v53
	v_cvt_pk_f16_f32 v42, v46, v47
	v_pk_fma_f32 v[40:41], v[40:41], s[16:17], v[248:249] op_sel_hi:[1,0,1]
	v_pk_fma_f32 v[38:39], v[38:39], s[16:17], v[246:247] op_sel_hi:[1,0,1]
	global_store_dwordx4 v[50:51], v[42:45], off
	v_pk_fma_f32 v[36:37], v[36:37], s[16:17], v[252:253] op_sel_hi:[1,0,1]
	v_pk_fma_f32 v[34:35], v[34:35], s[16:17], v[250:251] op_sel_hi:[1,0,1]
	v_mul_f32_e32 v42, v39, v39
	v_mul_f32_e32 v43, v41, v41
	v_fmac_f32_e32 v42, v38, v38
	v_fmac_f32_e32 v43, v40, v40
	v_add_f32_e32 v42, v42, v43
	v_mul_f32_e32 v43, v35, v35
	v_mul_f32_e32 v44, v37, v37
	v_fmac_f32_e32 v43, v34, v34
	v_fmac_f32_e32 v44, v36, v36
	v_add_f32_e32 v43, v43, v44
	v_add_f32_e32 v42, v42, v43
	v_med3_f32 v43, v38, s42, v165
	v_med3_f32 v38, v34, s42, v165
	v_add_f32_e32 v34, v52, v42
	v_med3_f32 v45, v35, s42, v165
	ds_bpermute_b32 v35, v167, v34
	v_med3_f32 v44, v39, s42, v165
	v_med3_f32 v40, v40, s42, v165
	v_med3_f32 v36, v36, s42, v165
	v_med3_f32 v41, v41, s42, v165
	s_waitcnt lgkmcnt(0)
	v_add_f32_e32 v34, v34, v35
	ds_bpermute_b32 v35, v166, v34
	v_med3_f32 v37, v37, s42, v165
	v_cvt_pk_f16_f32 v39, v36, v37
	v_cvt_pk_f16_f32 v37, v40, v41
	v_cvt_pk_f16_f32 v38, v38, v45
	v_cvt_pk_f16_f32 v36, v43, v44
	global_store_dwordx4 v[50:51], v[36:39], off offset:256
	s_and_saveexec_b64 s[0:1], s[6:7]
	s_cbranch_execz .LBB0_833
	v_lshlrev_b64 v[36:37], 7, v[82:83]
	v_lshl_add_u64 v[36:37], s[14:15], 0, v[36:37]
	s_waitcnt lgkmcnt(0)
	v_add_f32_e32 v34, v34, v35
	global_store_dword v[36:37], v34, off
;     __device__ __forceinline__ void operator()(const f32x4 (&acc)[2][2][4][2], const Unit& u, int wr, int wc, int fr, int fq, LAS const unsigned char* tbl, LAS const unsigned char* b2l) const {
;     ...
;             for (int mp = 0; mp < 2; ++mp) { f32x4 r[2][2][2];
; #pragma unroll
;                 for (int mm = 0; mm < 2; ++mm) { const size_t off = (size_t)(row0 + ai * HALF + (2 * mp + mm) * 16) * ldc + col0;
; #pragma unroll
;                     for (int bj = 0; bj < 2; ++bj)
; #pragma unroll
;                         for (int n = 0; n < 2; ++n) r[mm][bj][n] = __builtin_nontemporal_load((const f32x4*)(rp + off + bj * HALF + n * 4)); }
; #pragma unroll
;                 for (int mm = 0; mm < 2; ++mm) { const int m = 2 * mp + mm; const int row = row0 + ai * HALF + m * 16; const size_t off = (size_t)row * ldc + col0; float ss = 0.f;
; #pragma unroll
;                     for (int bj = 0; bj < 2; ++bj) { const f32x4 o0 = r[mm][bj][0] + acc[ai][bj][m][0] * scale, o1 = r[mm][bj][1] + acc[ai][bj][m][1] * scale;
;                         ss += ((o0[0] * o0[0] + o0[1] * o0[1]) + (o0[2] * o0[2] + o0[3] * o0[3])) + ((o1[0] * o1[0] + o1[1] * o1[1]) + (o1[2] * o1[2] + o1[3] * o1[3]));
;                         f16x8 h;
; #pragma unroll
;                         for (int j = 0; j < 4; ++j) { h[j] = (_Float16)__builtin_amdgcn_fmed3f(o0[j], -65504.0f, 65504.0f); h[4 + j] = (_Float16)__builtin_amdgcn_fmed3f(o1[j], -65504.0f, 65504.0f); }
;                         *(f16x8*)(cp + off + bj * HALF) = h; }
;                     ss += __shfl_xor(ss, 16); ss += __shfl_xor(ss, 32);
;                     if (fq == 0) rowss[(size_t)row * 32 + u.pn * 4 + wc] = ss; } }
.LBB0_833:
	s_or_b64 exec, exec, s[0:1]
	v_add_u32_e32 v52, 0xa0, v148
	v_ashrrev_i32_e32 v53, 31, v52
	s_waitcnt lgkmcnt(0)
	v_lshlrev_b64 v[34:35], 13, v[52:53]
	v_lshl_add_u64 v[34:35], v[150:151], 0, v[34:35]
	v_add_u32_e32 v50, 0xb0, v148
	v_ashrrev_i32_e32 v51, 31, v50
	v_lshlrev_b64 v[34:35], 13, v[50:51]
	v_lshl_add_u64 v[34:35], v[150:151], 0, v[34:35]
	v_lshlrev_b64 v[70:71], 12, v[52:53]
	v_lshl_add_u64 v[70:71], v[146:147], 0, v[70:71]
	s_waitcnt vmcnt(4) lgkmcnt(0)
	v_pk_fma_f32 v[24:25], v[24:25], s[16:17], v[192:193] op_sel_hi:[1,0,1]
	v_pk_fma_f32 v[22:23], v[22:23], s[16:17], v[190:191] op_sel_hi:[1,0,1]
	v_pk_fma_f32 v[20:21], v[20:21], s[16:17], v[196:197] op_sel_hi:[1,0,1]
	v_pk_fma_f32 v[18:19], v[18:19], s[16:17], v[194:195] op_sel_hi:[1,0,1]
	v_pk_fma_f32 v[32:33], v[32:33], s[16:17], v[200:201] op_sel_hi:[1,0,1]
	v_pk_fma_f32 v[30:31], v[30:31], s[16:17], v[198:199] op_sel_hi:[1,0,1]
	v_pk_fma_f32 v[28:29], v[28:29], s[16:17], v[204:205] op_sel_hi:[1,0,1]
	v_pk_fma_f32 v[26:27], v[26:27], s[16:17], v[202:203] op_sel_hi:[1,0,1]
	v_mul_f32_e32 v54, v23, v23
	v_mul_f32_e32 v55, v25, v25
	v_mul_f32_e32 v56, v19, v19
	v_mul_f32_e32 v57, v21, v21
	v_med3_f32 v58, v22, s42, v165
	v_med3_f32 v59, v18, s42, v165
	v_med3_f32 v23, v23, s42, v165
	v_med3_f32 v60, v19, s42, v165
	v_med3_f32 v19, v24, s42, v165
	v_med3_f32 v61, v20, s42, v165
	v_med3_f32 v25, v25, s42, v165
	v_med3_f32 v21, v21, s42, v165
	v_mul_f32_e32 v62, v31, v31
	v_mul_f32_e32 v63, v33, v33
	v_mul_f32_e32 v64, v27, v27
	v_mul_f32_e32 v65, v29, v29
	v_fmac_f32_e32 v54, v22, v22
	v_fmac_f32_e32 v55, v24, v24
	v_fmac_f32_e32 v56, v18, v18
	v_fmac_f32_e32 v57, v20, v20
	v_cvt_pk_f16_f32 v21, v61, v21
	v_cvt_pk_f16_f32 v19, v19, v25
	v_cvt_pk_f16_f32 v20, v59, v60
	v_cvt_pk_f16_f32 v18, v58, v23
	v_fmac_f32_e32 v62, v30, v30
	v_fmac_f32_e32 v63, v32, v32
	v_fmac_f32_e32 v64, v26, v26
	v_fmac_f32_e32 v65, v28, v28
	v_add_f32_e32 v22, v54, v55
	v_add_f32_e32 v23, v56, v57
	global_store_dwordx4 v[70:71], v[18:21], off
	v_med3_f32 v66, v30, s42, v165
	v_med3_f32 v67, v26, s42, v165
	v_add_f32_e32 v18, v62, v63
	v_add_f32_e32 v19, v64, v65
	v_add_f32_e32 v20, v22, v23
	v_add_f32_e32 v18, v18, v19
	v_add_f32_e32 v18, v20, v18
	ds_bpermute_b32 v19, v167, v18
	v_med3_f32 v31, v31, s42, v165
	v_med3_f32 v27, v27, s42, v165
	v_med3_f32 v21, v32, s42, v165
	v_med3_f32 v20, v28, s42, v165
	s_waitcnt lgkmcnt(0)
	v_add_f32_e32 v18, v18, v19
	ds_bpermute_b32 v19, v166, v18
	v_med3_f32 v22, v33, s42, v165
	v_med3_f32 v23, v29, s42, v165
	v_cvt_pk_f16_f32 v23, v20, v23
	v_cvt_pk_f16_f32 v21, v21, v22
	v_cvt_pk_f16_f32 v22, v67, v27
	v_cvt_pk_f16_f32 v20, v66, v31
	global_store_dwordx4 v[70:71], v[20:23], off offset:256
	s_and_saveexec_b64 s[0:1], s[6:7]
	s_cbranch_execz .LBB0_835
	v_lshlrev_b64 v[20:21], 7, v[52:53]
	v_lshl_add_u64 v[20:21], s[14:15], 0, v[20:21]
	s_waitcnt lgkmcnt(0)
	v_add_f32_e32 v18, v18, v19
	global_store_dword v[20:21], v18, off
.LBB0_835:
	s_or_b64 exec, exec, s[0:1]
	v_pk_fma_f32 v[8:9], v[8:9], s[16:17], v[208:209] op_sel_hi:[1,0,1]
	v_pk_fma_f32 v[6:7], v[6:7], s[16:17], v[206:207] op_sel_hi:[1,0,1]
	v_mul_f32_e32 v21, v9, v9
	v_mul_f32_e32 v20, v7, v7
	v_pk_fma_f32 v[4:5], v[4:5], s[16:17], v[212:213] op_sel_hi:[1,0,1]
	v_pk_fma_f32 v[2:3], v[2:3], s[16:17], v[210:211] op_sel_hi:[1,0,1]
	v_fmac_f32_e32 v20, v6, v6
	v_fmac_f32_e32 v21, v8, v8
	v_add_f32_e32 v20, v20, v21
	v_mul_f32_e32 v21, v3, v3
	v_mul_f32_e32 v22, v5, v5
	v_fmac_f32_e32 v21, v2, v2
	v_fmac_f32_e32 v22, v4, v4
	v_add_f32_e32 v21, v21, v22
	s_waitcnt lgkmcnt(0)
	v_lshlrev_b64 v[18:19], 11, v[50:51]
	v_add_f32_e32 v20, v20, v21
	v_med3_f32 v6, v6, s42, v165
	v_med3_f32 v2, v2, s42, v165
	v_med3_f32 v7, v7, s42, v165
	v_med3_f32 v21, v3, s42, v165
	v_med3_f32 v3, v8, s42, v165
	v_med3_f32 v4, v4, s42, v165
	v_med3_f32 v8, v9, s42, v165
	v_med3_f32 v5, v5, s42, v165
	v_lshl_add_u64 v[18:19], v[18:19], 1, v[146:147]
	v_cvt_pk_f16_f32 v5, v4, v5
	v_cvt_pk_f16_f32 v3, v3, v8
	v_cvt_pk_f16_f32 v4, v2, v21
	v_cvt_pk_f16_f32 v2, v6, v7
	global_store_dwordx4 v[18:19], v[2:5], off
	v_pk_fma_f32 v[8:9], v[10:11], s[16:17], v[218:219] op_sel_hi:[1,0,1]
	v_pk_fma_f32 v[6:7], v[12:13], s[16:17], v[220:221] op_sel_hi:[1,0,1]
	v_pk_fma_f32 v[2:3], v[16:17], s[16:17], v[216:217] op_sel_hi:[1,0,1]
	v_pk_fma_f32 v[4:5], v[14:15], s[16:17], v[214:215] op_sel_hi:[1,0,1]
	v_mul_f32_e32 v11, v3, v3
	v_mul_f32_e32 v10, v5, v5
	v_fmac_f32_e32 v10, v4, v4
	v_fmac_f32_e32 v11, v2, v2
	v_add_f32_e32 v10, v10, v11
	v_mul_f32_e32 v11, v9, v9
	v_mul_f32_e32 v12, v7, v7
	v_fmac_f32_e32 v11, v8, v8
	v_fmac_f32_e32 v12, v6, v6
	v_add_f32_e32 v11, v11, v12
	v_add_f32_e32 v10, v10, v11
	v_med3_f32 v11, v5, s42, v165
	v_med3_f32 v5, v2, s42, v165
	v_add_f32_e32 v2, v20, v10
	ds_bpermute_b32 v10, v167, v2
	v_med3_f32 v6, v6, s42, v165
	v_med3_f32 v12, v3, s42, v165
	v_med3_f32 v3, v7, s42, v165
	v_cvt_pk_f16_f32 v7, v6, v3
	s_waitcnt lgkmcnt(0)
	v_add_f32_e32 v2, v2, v10
	ds_bpermute_b32 v3, v166, v2
	v_med3_f32 v4, v4, s42, v165
	v_med3_f32 v8, v8, s42, v165
	v_med3_f32 v9, v9, s42, v165
	v_cvt_pk_f16_f32 v5, v5, v12
	v_cvt_pk_f16_f32 v6, v8, v9
	v_cvt_pk_f16_f32 v4, v4, v11
	global_store_dwordx4 v[18:19], v[4:7], off offset:256
	s_and_saveexec_b64 s[0:1], s[6:7]
	s_cbranch_execz .LBB0_810
	v_lshlrev_b64 v[4:5], 7, v[50:51]
	v_lshl_add_u64 v[4:5], s[14:15], 0, v[4:5]
	s_waitcnt lgkmcnt(0)
	v_add_f32_e32 v2, v2, v3
	global_store_dword v[4:5], v2, off
	s_branch .LBB0_810
